# grid barrier variant: the last arriver writes the new generation into every XCD's generation word with plain system-scope stores (no atomics); every other workgroup polls its own XCD's word (32 poller
# speedup vs baseline: 1.0091x; 1.0091x over previous
.LBB0_95:
	s_or_b64 exec, exec, s[8:9]
	s_and_saveexec_b64 s[8:9], s[12:13]
	s_cbranch_execz .LBB0_97
	v_add_u32_e32 v2, 1, v2
	v_mov_b32_e32 v3, 0x6400
	global_store_dword v3, v2, s[26:27] sc0 sc1
	global_store_dword v3, v2, s[26:27] offset:256 sc0 sc1
	global_store_dword v3, v2, s[26:27] offset:512 sc0 sc1
	global_store_dword v3, v2, s[26:27] offset:768 sc0 sc1
	global_store_dword v3, v2, s[26:27] offset:1024 sc0 sc1
	global_store_dword v3, v2, s[26:27] offset:1280 sc0 sc1
	global_store_dword v3, v2, s[26:27] offset:1536 sc0 sc1
	global_store_dword v3, v2, s[26:27] offset:1792 sc0 sc1
	global_store_dword v3, v2, s[26:27] offset:2048 sc0 sc1
	global_store_dword v3, v2, s[26:27] offset:2304 sc0 sc1
	global_store_dword v3, v2, s[26:27] offset:2560 sc0 sc1
	global_store_dword v3, v2, s[26:27] offset:2816 sc0 sc1
	global_store_dword v3, v2, s[26:27] offset:3072 sc0 sc1
	global_store_dword v3, v2, s[26:27] offset:3328 sc0 sc1
	global_store_dword v3, v2, s[26:27] offset:3584 sc0 sc1
	global_store_dword v3, v2, s[26:27] offset:3840 sc0 sc1
